# conversion-in-attention staggered by wave pair (two waves of a workgroup convert per iteration instead of all eight every 4th)
# speedup vs baseline: 1.0150x; 1.0150x over previous
; #define LAS __attribute__((address_space(3)))
; __device__ __forceinline__ void convert_experts(Frame& F, int lo, int hi) {
;     const int gw = F.vcu * 8 + F.wave, NGW = F.G * 8;
;     LAS unsigned char* scr = F.lds + F.wave * 16384;
;     unsigned char* W1t = WSP(F, WS_W1T, unsigned char); unsigned char* W2t = WSP(F, WS_W2T, unsigned char);
;     const float* weg = F.a->in[I_WEG]; const float* weu = F.a->in[I_WEU]; const float* wed = F.a->in[I_WED];
;     const float* wsg = F.a->in[I_WSG]; const float* wsu = F.a->in[I_WSU]; const float* wsd = F.a->in[I_WSD];
;     ...
;     constexpr int NPAIRS = CONV_ITEMS / 2;
;     (void)lo; (void)hi;
;     ...
;     if (gw < NPAIRS) {
;         const int ns = 2 * ((NPAIRS - gw + NGW - 1) / NGW);
;         int sq = 0, r = CONV_RIDX(0);
;         TItem tc, tn; CONV_DESC(r, tc); tn = tc;
;         int p = 0; bool first = true;
.Lcva_vcu:
	s_lshr_b32 s99, s99, 6
	s_lshl_b32 s101, s101, 3
	s_add_u32 s89, s101, s99
	s_movk_i32 s90, 12
	s_lshr_b32 s32, s99, 2
	s_xor_b32 s32, s32, s99
	s_lshr_b32 s100, s89, 3
	s_add_u32 s32, s32, s100
	s_and_b32 s32, s32, 3
	s_cmp_ge_u32 s32, 4
	s_cselect_b32 s99, 4, 0
	s_sub_u32 s32, s32, s99
	s_mov_b32 s95, 0
	s_waitcnt vmcnt(0)
	s_branch .LBB0_304
